# stack6_len24
# speedup vs baseline: 1.0022x; 1.0022x over previous
.LBB2_2:
	s_or_b64 exec, exec, s[12:13]
	v_lshrrev_b32_e32 v68, 7, v0
	s_lshl_b32 s0, s2, 4
	v_lshl_or_b32 v34, v68, 2, s0
	v_lshrrev_b32_e32 v2, 1, v0
	v_ashrrev_i32_e32 v35, 31, v34
	v_and_b32_e32 v69, 32, v2
	v_lshlrev_b64 v[2:3], 8, v[34:35]
	v_lshl_add_u64 v[2:3], s[4:5], 0, v[2:3]
	v_lshlrev_b32_e32 v66, 2, v69
	v_lshl_add_u64 v[2:3], v[2:3], 0, v[66:67]
	v_lshlrev_b32_e32 v36, 2, v1
	v_mov_b32_e32 v37, v67
	v_lshl_add_u64 v[2:3], v[2:3], 0, v[36:37]
	v_lshlrev_b32_e32 v38, 22, v72
	v_mov_b32_e32 v39, v67
	v_lshl_add_u64 v[4:5], v[2:3], 0, v[38:39]
	v_or_b32_e32 v40, 0x800000, v38
	v_mov_b32_e32 v41, v67
	global_load_dword v6, v[4:5], off
	v_lshl_add_u64 v[4:5], v[2:3], 0, v[40:41]
	v_or_b32_e32 v42, 0x1000000, v38
	v_mov_b32_e32 v43, v67
	global_load_dword v18, v[4:5], off
	v_lshl_add_u64 v[4:5], v[2:3], 0, v[42:43]
	v_or_b32_e32 v44, 0x1800000, v38
	v_mov_b32_e32 v45, v67
	global_load_dword v19, v[4:5], off
	v_lshl_add_u64 v[4:5], v[2:3], 0, v[44:45]
	v_or_b32_e32 v46, 0x2000000, v38
	v_mov_b32_e32 v47, v67
	global_load_dword v20, v[4:5], off
	v_lshl_add_u64 v[4:5], v[2:3], 0, v[46:47]
	v_or_b32_e32 v48, 0x2800000, v38
	v_mov_b32_e32 v49, v67
	global_load_dword v21, v[4:5], off
	v_lshl_add_u64 v[4:5], v[2:3], 0, v[48:49]
	v_or_b32_e32 v50, 0x3000000, v38
	v_mov_b32_e32 v51, v67
	global_load_dword v22, v[4:5], off
	v_lshl_add_u64 v[4:5], v[2:3], 0, v[50:51]
	v_or_b32_e32 v52, 0x3800000, v38
	v_mov_b32_e32 v53, v67
	global_load_dword v23, v[4:5], off
	v_lshl_add_u64 v[4:5], v[2:3], 0, v[52:53]
	v_or_b32_e32 v54, 0x4000000, v38
	v_mov_b32_e32 v55, v67
	global_load_dword v24, v[4:5], off
	v_lshl_add_u64 v[4:5], v[2:3], 0, v[54:55]
	v_or_b32_e32 v56, 0x4800000, v38
	v_mov_b32_e32 v57, v67
	global_load_dword v25, v[4:5], off
	v_lshl_add_u64 v[4:5], v[2:3], 0, v[56:57]
	v_or_b32_e32 v58, 0x5000000, v38
	v_mov_b32_e32 v59, v67
	global_load_dword v26, v[4:5], off
	v_lshl_add_u64 v[4:5], v[2:3], 0, v[58:59]
	v_or_b32_e32 v60, 0x5800000, v38
	v_mov_b32_e32 v61, v67
	s_mov_b64 s[6:7], 0x6000000
	global_load_dword v27, v[4:5], off
	v_lshl_add_u64 v[4:5], v[2:3], 0, v[60:61]
	v_lshl_add_u64 v[2:3], v[2:3], 0, s[6:7]
	global_load_dword v28, v[4:5], off
	global_load_dword v29, v[2:3], off
	v_or_b32_e32 v2, 1, v34
	v_ashrrev_i32_e32 v3, 31, v2
	v_lshlrev_b64 v[2:3], 8, v[2:3]
	v_lshl_add_u64 v[2:3], s[4:5], 0, v[2:3]
	v_lshl_add_u64 v[2:3], v[2:3], 0, v[66:67]
	v_lshl_add_u64 v[2:3], v[2:3], 0, v[36:37]
	v_lshl_add_u64 v[4:5], v[2:3], 0, v[38:39]
	global_load_dword v30, v[4:5], off
	v_lshl_add_u64 v[4:5], v[2:3], 0, v[40:41]
	global_load_dword v35, v[4:5], off
	v_lshl_add_u64 v[4:5], v[2:3], 0, v[42:43]
	global_load_dword v63, v[4:5], off
	v_lshl_add_u64 v[4:5], v[2:3], 0, v[44:45]
	global_load_dword v64, v[4:5], off
	v_lshl_add_u64 v[4:5], v[2:3], 0, v[46:47]
	global_load_dword v65, v[4:5], off
	v_lshl_add_u64 v[4:5], v[2:3], 0, v[48:49]
	global_load_dword v83, v[4:5], off
	v_lshl_add_u64 v[4:5], v[2:3], 0, v[50:51]
	global_load_dword v84, v[4:5], off
	v_lshl_add_u64 v[4:5], v[2:3], 0, v[52:53]
	global_load_dword v85, v[4:5], off
	v_lshl_add_u64 v[4:5], v[2:3], 0, v[54:55]
	global_load_dword v86, v[4:5], off
	v_lshl_add_u64 v[4:5], v[2:3], 0, v[56:57]
	global_load_dword v87, v[4:5], off
	v_lshl_add_u64 v[4:5], v[2:3], 0, v[58:59]
	global_load_dword v88, v[4:5], off
	v_lshl_add_u64 v[4:5], v[2:3], 0, v[60:61]
	global_load_dword v89, v[4:5], off
	v_lshl_add_u64 v[2:3], v[2:3], 0, s[6:7]
	global_load_dword v90, v[2:3], off
	s_waitcnt vmcnt(13)
	s_mov_b32 s0, 0xff61b1e6
	v_mfma_f32_32x32x2_f32 v[2:17], v62, v6, 0
	v_or_b32_e32 v1, v69, v1
	v_lshlrev_b32_e32 v1, 9, v1
	v_mfma_f32_32x32x2_f32 v[2:17], v82, v18, v[2:17]
	v_or_b32_e32 v18, 2, v34
	v_or_b32_e32 v34, 3, v34
	v_mfma_f32_32x32x2_f32 v[2:17], v81, v19, v[2:17]
	v_ashrrev_i32_e32 v19, 31, v18
	v_lshlrev_b64 v[18:19], 8, v[18:19]
	v_lshl_add_u64 v[18:19], s[4:5], 0, v[18:19]
	v_lshl_add_u64 v[18:19], v[18:19], 0, v[66:67]
	v_lshl_add_u64 v[18:19], v[18:19], 0, v[36:37]
	v_mfma_f32_32x32x2_f32 v[2:17], v80, v20, v[2:17]
	v_mfma_f32_32x32x2_f32 v[2:17], v79, v21, v[2:17]
	v_lshl_add_u64 v[20:21], v[18:19], 0, v[38:39]
	global_load_dword v91, v[20:21], off
	v_lshl_add_u64 v[20:21], v[18:19], 0, v[40:41]
	global_load_dword v92, v[20:21], off
	v_lshl_add_u64 v[20:21], v[18:19], 0, v[42:43]
	global_load_dword v93, v[20:21], off
	v_lshl_add_u64 v[20:21], v[18:19], 0, v[44:45]
	global_load_dword v94, v[20:21], off
	v_lshl_add_u64 v[20:21], v[18:19], 0, v[46:47]
	global_load_dword v95, v[20:21], off
	v_lshl_add_u64 v[20:21], v[18:19], 0, v[48:49]
	global_load_dword v96, v[20:21], off
	v_lshl_add_u64 v[20:21], v[18:19], 0, v[50:51]
	global_load_dword v97, v[20:21], off
	v_lshl_add_u64 v[20:21], v[18:19], 0, v[52:53]
	v_mfma_f32_32x32x2_f32 v[2:17], v78, v22, v[2:17]
	global_load_dword v98, v[20:21], off
	v_lshl_add_u64 v[20:21], v[18:19], 0, v[54:55]
	global_load_dword v99, v[20:21], off
	v_lshl_add_u64 v[20:21], v[18:19], 0, v[56:57]
	global_load_dword v100, v[20:21], off
	v_lshl_add_u64 v[20:21], v[18:19], 0, v[58:59]
	global_load_dword v101, v[20:21], off
	v_lshl_add_u64 v[20:21], v[18:19], 0, v[60:61]
	global_load_dword v102, v[20:21], off
	v_lshl_add_u64 v[18:19], v[18:19], 0, s[6:7]
	global_load_dword v103, v[18:19], off
	s_waitcnt vmcnt(13)
	v_mfma_f32_32x32x2_f32 v[2:17], v77, v23, v[2:17]
	v_mfma_f32_32x32x2_f32 v[2:17], v76, v24, v[2:17]
	v_mfma_f32_32x32x2_f32 v[2:17], v75, v25, v[2:17]
	v_mfma_f32_32x32x2_f32 v[2:17], v74, v26, v[2:17]
	v_mfma_f32_32x32x2_f32 v[2:17], v73, v27, v[2:17]
	v_mfma_f32_32x32x2_f32 v[2:17], v71, v28, v[2:17]
	v_mfma_f32_32x32x2_f32 v[2:17], v70, v29, v[2:17]
	v_mfma_f32_32x32x2_f32 v[18:33], v62, v30, 0
	v_mfma_f32_32x32x2_f32 v[18:33], v82, v35, v[18:33]
	v_ashrrev_i32_e32 v35, 31, v34
	v_lshlrev_b64 v[34:35], 8, v[34:35]
	v_lshl_add_u64 v[34:35], s[4:5], 0, v[34:35]
	v_lshl_add_u64 v[34:35], v[34:35], 0, v[66:67]
	v_lshl_add_u64 v[34:35], v[34:35], 0, v[36:37]
	v_lshl_add_u64 v[36:37], v[34:35], 0, v[38:39]
	v_mfma_f32_32x32x2_f32 v[18:33], v81, v63, v[18:33]
	global_load_dword v63, v[36:37], off
	v_lshl_add_u64 v[36:37], v[34:35], 0, v[40:41]
	global_load_dword v66, v[36:37], off
	v_lshl_add_u64 v[36:37], v[34:35], 0, v[42:43]
	v_mfma_f32_32x32x2_f32 v[18:33], v80, v64, v[18:33]
	v_mfma_f32_32x32x2_f32 v[18:33], v79, v65, v[18:33]
	v_mfma_f32_32x32x2_f32 v[18:33], v78, v83, v[18:33]
	global_load_dword v83, v[36:37], off
	v_lshl_add_u64 v[36:37], v[34:35], 0, v[44:45]
	v_mfma_f32_32x32x2_f32 v[18:33], v77, v84, v[18:33]
	global_load_dword v84, v[36:37], off
	v_lshl_add_u64 v[36:37], v[34:35], 0, v[46:47]
	v_mfma_f32_32x32x2_f32 v[18:33], v76, v85, v[18:33]
	global_load_dword v85, v[36:37], off
	v_lshl_add_u64 v[36:37], v[34:35], 0, v[48:49]
	v_mfma_f32_32x32x2_f32 v[18:33], v75, v86, v[18:33]
	global_load_dword v86, v[36:37], off
	v_lshl_add_u64 v[36:37], v[34:35], 0, v[50:51]
	v_mfma_f32_32x32x2_f32 v[18:33], v74, v87, v[18:33]
	global_load_dword v87, v[36:37], off
	v_lshl_add_u64 v[36:37], v[34:35], 0, v[52:53]
	v_mfma_f32_32x32x2_f32 v[18:33], v73, v88, v[18:33]
	global_load_dword v88, v[36:37], off
	v_lshl_add_u64 v[36:37], v[34:35], 0, v[54:55]
	v_mfma_f32_32x32x2_f32 v[18:33], v71, v89, v[18:33]
	global_load_dword v89, v[36:37], off
	v_lshl_add_u64 v[36:37], v[34:35], 0, v[56:57]
	v_mfma_f32_32x32x2_f32 v[18:33], v70, v90, v[18:33]
	global_load_dword v90, v[36:37], off
	v_lshl_add_u64 v[36:37], v[34:35], 0, v[58:59]
	global_load_dword v104, v[36:37], off
	v_lshl_add_u64 v[36:37], v[34:35], 0, v[60:61]
	global_load_dword v105, v[36:37], off
	v_lshl_add_u64 v[34:35], v[34:35], 0, s[6:7]
	global_load_dword v106, v[34:35], off
	s_waitcnt vmcnt(13)
	s_nop 14
	v_max3_f32 v2, v2, s0, v18
	s_waitcnt vmcnt(0)
	v_mfma_f32_32x32x2_f32 v[34:49], v62, v91, 0
	v_max3_f32 v3, v3, s0, v19
	v_max3_f32 v4, v4, s0, v20
	v_max3_f32 v5, v5, s0, v21
	v_max3_f32 v6, v6, s0, v22
	v_max3_f32 v7, v7, s0, v23
	v_max3_f32 v8, v8, s0, v24
	v_max3_f32 v9, v9, s0, v25
	v_lshlrev_b32_e32 v18, 5, v68
	v_max3_f32 v10, v10, s0, v26
	v_max3_f32 v11, v11, s0, v27
	v_max3_f32 v12, v12, s0, v28
	v_max3_f32 v13, v13, s0, v29
	v_max3_f32 v14, v14, s0, v30
	v_max3_f32 v15, v15, s0, v31
	v_max3_f32 v16, v16, s0, v32
	v_mfma_f32_32x32x2_f32 v[50:65], v62, v63, 0
	v_max3_f32 v17, v17, s0, v33
	s_lshl_b32 s0, s2, 2
	s_mov_b32 s2, 0x7f000
	v_mfma_f32_32x32x2_f32 v[34:49], v82, v92, v[34:49]
	v_mfma_f32_32x32x2_f32 v[50:65], v82, v66, v[50:65]
	v_lshlrev_b32_e32 v66, 4, v72
	v_or3_b32 v1, v1, v18, v66
	v_mfma_f32_32x32x2_f32 v[34:49], v81, v93, v[34:49]
	v_mfma_f32_32x32x2_f32 v[50:65], v81, v83, v[50:65]
	v_mfma_f32_32x32x2_f32 v[34:49], v80, v94, v[34:49]
	v_mfma_f32_32x32x2_f32 v[50:65], v80, v84, v[50:65]
	v_mfma_f32_32x32x2_f32 v[34:49], v79, v95, v[34:49]
	v_mfma_f32_32x32x2_f32 v[50:65], v79, v85, v[50:65]
	v_mfma_f32_32x32x2_f32 v[34:49], v78, v96, v[34:49]
	v_mfma_f32_32x32x2_f32 v[50:65], v78, v86, v[50:65]
	v_mfma_f32_32x32x2_f32 v[34:49], v77, v97, v[34:49]
	v_mfma_f32_32x32x2_f32 v[50:65], v77, v87, v[50:65]
	v_mfma_f32_32x32x2_f32 v[34:49], v76, v98, v[34:49]
	v_mfma_f32_32x32x2_f32 v[50:65], v76, v88, v[50:65]
	v_mfma_f32_32x32x2_f32 v[34:49], v75, v99, v[34:49]
	v_mfma_f32_32x32x2_f32 v[50:65], v75, v89, v[50:65]
	v_mfma_f32_32x32x2_f32 v[34:49], v74, v100, v[34:49]
	v_mfma_f32_32x32x2_f32 v[50:65], v74, v90, v[50:65]
	global_load_dwordx4 v[74:77], v66, s[8:9]
	global_load_dwordx4 v[78:81], v66, s[8:9] offset:32
	global_load_dwordx4 v[82:85], v66, s[8:9] offset:64
	global_load_dwordx4 v[86:89], v66, s[8:9] offset:96
	v_mfma_f32_32x32x2_f32 v[34:49], v73, v101, v[34:49]
	v_mfma_f32_32x32x2_f32 v[50:65], v73, v104, v[50:65]
	v_mfma_f32_32x32x2_f32 v[34:49], v71, v102, v[34:49]
	v_mfma_f32_32x32x2_f32 v[50:65], v71, v105, v[50:65]
	v_mfma_f32_32x32x2_f32 v[34:49], v70, v103, v[34:49]
	v_mfma_f32_32x32x2_f32 v[50:65], v70, v106, v[50:65]
	s_nop 15
	s_nop 1
	v_max3_f32 v2, v2, v34, v50
	v_max3_f32 v3, v3, v35, v51
	v_max3_f32 v4, v4, v36, v52
	v_max3_f32 v5, v5, v37, v53
	s_waitcnt vmcnt(3)
	v_add_f32_e32 v2, v2, v74
	v_add_f32_e32 v3, v3, v75
	v_add_f32_e32 v4, v4, v76
	v_add_f32_e32 v5, v5, v77
	v_max3_f32 v6, v6, v38, v54
	v_max3_f32 v7, v7, v39, v55
	v_max3_f32 v8, v8, v40, v56
	v_max3_f32 v9, v9, v41, v57
	v_max_f32_e32 v2, 0, v2
	v_max_f32_e32 v3, 0, v3
	v_max_f32_e32 v4, 0, v4
	v_max_f32_e32 v5, 0, v5
	ds_write_b128 v1, v[2:5]
	s_waitcnt vmcnt(2)
	v_add_f32_e32 v2, v6, v78
	v_add_f32_e32 v3, v7, v79
	v_add_f32_e32 v4, v8, v80
	v_add_f32_e32 v5, v9, v81
	v_max3_f32 v10, v10, v42, v58
	v_max3_f32 v11, v11, v43, v59
	v_max3_f32 v12, v12, v44, v60
	v_max3_f32 v13, v13, v45, v61
	v_max_f32_e32 v2, 0, v2
	v_max_f32_e32 v3, 0, v3
	v_max_f32_e32 v4, 0, v4
	v_max_f32_e32 v5, 0, v5
	ds_write_b128 v1, v[2:5] offset:128
	s_waitcnt vmcnt(1)
	v_add_f32_e32 v2, v10, v82
	v_add_f32_e32 v3, v11, v83
	v_add_f32_e32 v4, v12, v84
	v_add_f32_e32 v5, v13, v85
	v_max3_f32 v14, v14, v46, v62
	v_max3_f32 v15, v15, v47, v63
	v_max3_f32 v16, v16, v48, v64
	v_max3_f32 v17, v17, v49, v65
	v_max_f32_e32 v2, 0, v2
	v_max_f32_e32 v3, 0, v3
	v_max_f32_e32 v4, 0, v4
	v_max_f32_e32 v5, 0, v5
	ds_write_b128 v1, v[2:5] offset:256
	s_waitcnt vmcnt(0)
	v_add_f32_e32 v2, v14, v86
	v_add_f32_e32 v3, v15, v87
	v_add_f32_e32 v4, v16, v88
	v_add_f32_e32 v5, v17, v89
	v_max_f32_e32 v2, 0, v2
	v_max_f32_e32 v3, 0, v3
	v_max_f32_e32 v4, 0, v4
	v_max_f32_e32 v5, 0, v5
	v_lshlrev_b32_e32 v12, 4, v0
	ds_write_b128 v1, v[2:5] offset:384
	s_waitcnt lgkmcnt(0)
	s_barrier
	v_and_b32_e32 v66, 0x70, v12
	v_lshlrev_b32_e32 v13, 9, v0
	ds_read_b128 v[0:3], v12
	v_lshl_add_u64 v[8:9], s[10:11], 0, v[66:67]
	v_and_b32_e32 v66, 0x3f000, v13
	v_lshl_add_u64 v[4:5], v[66:67], 0, s[0:1]
	v_lshlrev_b64 v[4:5], 5, v[4:5]
	v_lshl_add_u64 v[10:11], v[8:9], 0, v[4:5]
	ds_read_b128 v[4:7], v12 offset:8192
	s_waitcnt lgkmcnt(1)
	global_store_dwordx4 v[10:11], v[0:3], off sc1
	s_nop 1
	v_mov_b32_e32 v0, 0x40000
	v_bitop3_b32 v66, v13, s2, v0 bitop3:0xc8
	v_lshl_add_u64 v[0:1], v[66:67], 0, s[0:1]
	v_lshlrev_b64 v[0:1], 5, v[0:1]
	v_lshl_add_u64 v[0:1], v[8:9], 0, v[0:1]
	s_waitcnt lgkmcnt(0)
	global_store_dwordx4 v[0:1], v[4:7], off sc1
	s_mov_b32 s2, 0xbf000
	v_mov_b32_e32 v0, 0x80000
	v_bitop3_b32 v66, v13, s2, v0 bitop3:0xc8
	ds_read_b128 v[0:3], v12 offset:16384
	v_lshl_add_u64 v[4:5], v[66:67], 0, s[0:1]
	v_lshlrev_b64 v[4:5], 5, v[4:5]
	v_lshl_add_u64 v[10:11], v[8:9], 0, v[4:5]
	ds_read_b128 v[4:7], v12 offset:24576
	s_waitcnt lgkmcnt(1)
	global_store_dwordx4 v[10:11], v[0:3], off sc1
	s_mov_b32 s2, 0xff000
	s_nop 0
	v_mov_b32_e32 v0, 0xc0000
	v_bitop3_b32 v66, v13, s2, v0 bitop3:0xc8
	v_lshl_add_u64 v[0:1], v[66:67], 0, s[0:1]
	v_lshlrev_b64 v[0:1], 5, v[0:1]
	v_lshl_add_u64 v[0:1], v[8:9], 0, v[0:1]
	s_waitcnt lgkmcnt(0)
	global_store_dwordx4 v[0:1], v[4:7], off sc1
	s_barrier
	s_lshr_b32 s2, s0, 2
	s_cmp_gt_u32 s2, 63
	s_cbranch_scc1 .Lro_done
	v_lshrrev_b32_e32 v0, 4, v12
	v_cmp_gt_u32_e32 vcc, 64, v0
	s_and_saveexec_b64 s[4:5], vcc
	s_cbranch_execz .Lro_done
	s_lshl_b32 s3, s2, 2
	s_add_u32 s6, s10, 0x2050600
	s_addc_u32 s7, s11, 0
	s_add_u32 s6, s6, s3
	s_addc_u32 s7, s7, 0
	s_load_dword s14, s[6:7], 0x0
	s_load_dword s15, s[6:7], 0x100
	s_add_u32 s16, s10, 0x2050900
	s_addc_u32 s17, s11, 0
	v_and_b32_e32 v2, 15, v0
	v_mov_b32_e32 v11, 0
	s_mov_b32 s35, 0x10001
	v_cmp_lt_u32_e32 vcc, 3, v2
	s_nop 1
	v_cndmask_b32_e64 v30, 0, 8, vcc
	v_cmp_lt_u32_e32 vcc, 7, v2
	v_mov_b32_e32 v29, 12
	s_nop 0
	v_cndmask_b32_e32 v30, v30, v29, vcc
	v_cndmask_b32_e64 v31, 4, 8, vcc
	v_cmp_lt_u32_e32 vcc, 11, v2
	v_and_b32_e32 v28, 16, v0
	s_nop 0
	v_cndmask_b32_e64 v31, v31, 16, vcc
	v_cmp_ne_u32_e32 vcc, 0, v28
	v_and_b32_e32 v1, 32, v0
	s_nop 0
	v_cndmask_b32_e32 v30, v30, v31, vcc
	v_add3_u32 v1, v1, v2, v30
	v_lshlrev_b32_e32 v8, 3, v0
	v_lshlrev_b32_e32 v9, 2, v0
	v_add_u32_e32 v9, 0x2000, v9
	v_lshlrev_b32_e32 v10, 4, v1
	v_mov_b32_e32 v24, 0
	v_mov_b32_e32 v25, 0
	ds_write_b64 v8, v[24:25] offset:0
	ds_write_b64 v8, v[24:25] offset:512
	ds_write_b64 v8, v[24:25] offset:1024
	ds_write_b64 v8, v[24:25] offset:1536
	ds_write_b64 v8, v[24:25] offset:2048
	ds_write_b64 v8, v[24:25] offset:2560
	ds_write_b64 v8, v[24:25] offset:3072
	ds_write_b64 v8, v[24:25] offset:3584
	ds_write_b64 v8, v[24:25] offset:4096
	ds_write_b64 v8, v[24:25] offset:4608
	ds_write_b64 v8, v[24:25] offset:5120
	ds_write_b64 v8, v[24:25] offset:5632
	ds_write_b64 v8, v[24:25] offset:6144
	ds_write_b64 v8, v[24:25] offset:6656
	ds_write_b64 v8, v[24:25] offset:7168
	ds_write_b64 v8, v[24:25] offset:7680
	v_mov_b32_e32 v7, 0
	v_mov_b32_e32 v6, 0
	s_waitcnt lgkmcnt(0)
	s_cmp_eq_u32 s14, 0
	s_cbranch_scc1 .Lro_done
	s_cmp_gt_u32 s14, 24
	s_cbranch_scc1 .Lro_done
	s_lshl_b32 s15, s15, 2
	s_add_u32 s16, s16, s15
	s_addc_u32 s17, s17, 0
	s_mov_b64 s[18:19], s[16:17]
	s_cmp_le_u32 s14, 0
	s_cbranch_scc1 .Lro_loaded
	global_load_dwordx4 v[32:35], v10, s[18:19]
	s_add_u32 s18, s18, 0x400
	s_addc_u32 s19, s19, 0
	s_cmp_le_u32 s14, 4
	s_cbranch_scc1 .Lro_loaded
	global_load_dwordx4 v[36:39], v10, s[18:19]
	s_add_u32 s18, s18, 0x400
	s_addc_u32 s19, s19, 0
	s_cmp_le_u32 s14, 8
	s_cbranch_scc1 .Lro_loaded
	global_load_dwordx4 v[40:43], v10, s[18:19]
	s_add_u32 s18, s18, 0x400
	s_addc_u32 s19, s19, 0
	s_cmp_le_u32 s14, 12
	s_cbranch_scc1 .Lro_loaded
	global_load_dwordx4 v[44:47], v10, s[18:19]
	s_add_u32 s18, s18, 0x400
	s_addc_u32 s19, s19, 0
	s_cmp_le_u32 s14, 16
	s_cbranch_scc1 .Lro_loaded
	global_load_dwordx4 v[48:51], v10, s[18:19]
	s_add_u32 s18, s18, 0x400
	s_addc_u32 s19, s19, 0
	s_cmp_le_u32 s14, 20
	s_cbranch_scc1 .Lro_loaded
	global_load_dwordx4 v[52:55], v10, s[18:19]
	s_add_u32 s18, s18, 0x400
	s_addc_u32 s19, s19, 0
	s_cmp_le_u32 s14, 24
	s_cbranch_scc1 .Lro_loaded
	global_load_dwordx4 v[56:59], v10, s[18:19]
	s_add_u32 s18, s18, 0x400
	s_addc_u32 s19, s19, 0
	s_cmp_le_u32 s14, 28
	s_cbranch_scc1 .Lro_loaded
	global_load_dwordx4 v[60:63], v10, s[18:19]
	s_add_u32 s18, s18, 0x400
	s_addc_u32 s19, s19, 0
	s_cmp_le_u32 s14, 32
	s_cbranch_scc1 .Lro_loaded
	global_load_dwordx4 v[64:67], v10, s[18:19]
	s_add_u32 s18, s18, 0x400
	s_addc_u32 s19, s19, 0
	s_cmp_le_u32 s14, 36
	s_cbranch_scc1 .Lro_loaded
	global_load_dwordx4 v[68:71], v10, s[18:19]
	s_add_u32 s18, s18, 0x400
	s_addc_u32 s19, s19, 0
	s_cmp_le_u32 s14, 40
	s_cbranch_scc1 .Lro_loaded
	global_load_dwordx4 v[72:75], v10, s[18:19]
	s_add_u32 s18, s18, 0x400
	s_addc_u32 s19, s19, 0
	s_cmp_le_u32 s14, 44
	s_cbranch_scc1 .Lro_loaded
	global_load_dwordx4 v[76:79], v10, s[18:19]
	s_add_u32 s18, s18, 0x400
	s_addc_u32 s19, s19, 0
	s_cmp_le_u32 s14, 48
	s_cbranch_scc1 .Lro_loaded
	global_load_dwordx4 v[80:83], v10, s[18:19]
	s_add_u32 s18, s18, 0x400
	s_addc_u32 s19, s19, 0
	s_cmp_le_u32 s14, 52
	s_cbranch_scc1 .Lro_loaded
	global_load_dwordx4 v[84:87], v10, s[18:19]
	s_add_u32 s18, s18, 0x400
	s_addc_u32 s19, s19, 0
	s_cmp_le_u32 s14, 56
	s_cbranch_scc1 .Lro_loaded
	global_load_dwordx4 v[88:91], v10, s[18:19]
	s_add_u32 s18, s18, 0x400
	s_addc_u32 s19, s19, 0
	s_cmp_le_u32 s14, 60
	s_cbranch_scc1 .Lro_loaded
	global_load_dwordx4 v[92:95], v10, s[18:19]
	s_add_u32 s18, s18, 0x400
	s_addc_u32 s19, s19, 0
